# speedup vs baseline: 1.0053x; 1.0053x over previous
.Lattn_prio_done:
.LBB2_5:
	s_add_i32 s26, s26, 2
	v_add_u32_e32 v191, s3, v187
	ds_read_b64_tr_b16 v[176:177], v191 offset:24576
	ds_read_b64_tr_b16 v[178:179], v191 offset:25088
	v_mfma_f32_32x32x16_f16 v[96:111], v[172:175], v[124:127], v[32:47]
	v_exp_f32_e32 v56, v56
	v_exp_f32_e32 v57, v57
	v_cvt_pk_f16_f32 v140, v64, v65
	v_cvt_pk_f16_f32 v141, v66, v67
	ds_read_b64_tr_b16 v[172:173], v191 offset:28672
	ds_read_b64_tr_b16 v[174:175], v191 offset:29184
	v_mfma_f32_32x32x16_f16 v[80:95], v[168:171], v[124:127], v[32:47]
	v_exp_f32_e32 v58, v58
	v_exp_f32_e32 v59, v59
	v_pk_add_f16 v128, v140, v141
	v_cvt_pk_f16_f32 v142, v68, v69
	v_cvt_pk_f16_f32 v143, v70, v71
	ds_read_b64_tr_b16 v[64:65], v191 offset:25600
	ds_read_b64_tr_b16 v[66:67], v191 offset:26112
	v_mfma_f32_32x32x16_f16 v[96:111], v[164:167], v[120:123], v[96:111]
	v_exp_f32_e32 v60, v60
	v_exp_f32_e32 v61, v61
	v_pk_add_f16 v129, v142, v143
	v_cvt_pk_f16_f32 v136, v72, v73
	v_cvt_pk_f16_f32 v137, v74, v75
	ds_read_b64_tr_b16 v[68:69], v191 offset:29696
	ds_read_b64_tr_b16 v[70:71], v191 offset:30208
	v_mfma_f32_32x32x16_f16 v[80:95], v[160:163], v[120:123], v[80:95]
	v_exp_f32_e32 v62, v62
	v_exp_f32_e32 v63, v63
	v_pk_add_f16 v72, v136, v137
	v_pk_add_f16 v128, v128, v129
	v_cvt_pk_f16_f32 v138, v76, v77
	v_cvt_pk_f16_f32 v139, v78, v79
	s_add_i32 m0, s31, s24
	s_min_u32 s2, s26, 28
	s_lshl_b32 s2, s2, 13
	s_add_u32 s2, s14, s2
	s_addc_u32 s3, s15, 0
	s_add_u32 s2, s2, 0x6000
	s_addc_u32 s3, s3, 0
	global_load_lds_dwordx4 v189, s[2:3]
	ds_read_b64_tr_b16 v[76:77], v191 offset:26624
	ds_read_b64_tr_b16 v[78:79], v191 offset:27136
	v_mfma_f32_32x32x16_f16 v[96:111], v[156:159], v[116:119], v[96:111]
	v_pk_add_f16 v73, v138, v139
	v_cvt_pk_f16_f32 v132, v48, v49
	v_cvt_pk_f16_f32 v133, v50, v51
	ds_read_b64_tr_b16 v[48:49], v191 offset:30720
	ds_read_b64_tr_b16 v[50:51], v191 offset:31232
	v_mfma_f32_32x32x16_f16 v[80:95], v[152:155], v[116:119], v[80:95]
	v_pk_add_f16 v129, v72, v73
	v_cvt_pk_f16_f32 v134, v52, v53
	v_cvt_pk_f16_f32 v135, v54, v55
	v_pk_add_f16 v156, v132, v133
	s_add_i32 m0, s29, s25
	s_add_u32 s2, s27, 0x2000
	s_addc_u32 s3, s28, 0
	global_load_lds_dwordx4 v189, s[2:3]
	ds_read_b64_tr_b16 v[72:73], v191 offset:27648
	ds_read_b64_tr_b16 v[74:75], v191 offset:28160
	v_mfma_f32_32x32x16_f16 v[96:111], v[148:151], v[112:115], v[96:111]
	v_pk_add_f16 v153, v128, v129
	v_cvt_pk_f16_f32 v128, v56, v57
	v_cvt_pk_f16_f32 v129, v58, v59
	v_pk_add_f16 v152, v134, v135
	ds_read_b64_tr_b16 v[52:53], v191 offset:31744
	ds_read_b64_tr_b16 v[54:55], v191 offset:32256
	v_mfma_f32_32x32x16_f16 v[80:95], v[144:147], v[112:115], v[80:95]
	v_pk_add_f16 v56, v128, v129
	v_pk_add_f16 v57, v156, v152
	v_cvt_pk_f16_f32 v130, v60, v61
	v_cvt_pk_f16_f32 v131, v62, v63
	s_andn2_b64 vcc, exec, s[18:19]
	v_pk_add_f16 v57, v153, v57
	v_pk_add_f16 v58, v130, v131
	s_cbranch_vccnz .LBB2_7
	v_pk_add_f16 v59, v56, v58
	v_max3_f32 v61, v96, v97, v80
	v_max3_f32 v62, v98, v99, v81
	s_mov_b64 s[8:9], 0
	v_pk_add_f16 v59, v57, v59
	s_nop 0
	v_cvt_f32_f16_e32 v60, v59
	v_cvt_f32_f16_sdwa v59, v59 dst_sel:DWORD dst_unused:UNUSED_PAD src0_sel:WORD_1
	v_add_f32_e32 v59, v59, v60
	v_add_f32_e32 v188, v188, v59
	v_max3_f32 v59, v61, v82, v83
	v_max3_f32 v60, v62, v102, v103
	s_nop 0
	v_max3_f32 v59, v59, v100, v101
	v_max3_f32 v60, v60, v86, v87
	s_nop 0
	v_max3_f32 v59, v59, v84, v85
	v_max3_f32 v60, v60, v106, v107
	s_nop 0
	v_max3_f32 v59, v59, v104, v105
	v_max3_f32 v60, v60, v90, v91
	s_nop 0
	v_max3_f32 v59, v59, v88, v89
	v_max3_f32 v60, v60, v110, v111
	s_nop 0
	v_max3_f32 v59, v59, v108, v109
	v_max3_f32 v60, v60, v94, v95
	s_nop 0
	v_max3_f32 v59, v59, v92, v93
	s_nop 0
	v_max_f32 v59, v59, v60
	s_nop 0
	v_mov_b32_e32 v60, v59
	s_nop 1
	v_permlane32_swap_b32_e32 v59, v60
	v_max_f32 v59, v59, v60
	s_nop 0
	v_cmp_lt_f32_e32 vcc, s30, v59
	s_cbranch_vccnz .LBB2_19

.LBB2_11:
	s_add_i32 s33, s29, 0x2000
	s_cmpk_lg_i32 s29, 0x4000
	s_cselect_b32 s33, s33, 0
	v_add_u32_e32 v191, s31, v187
	ds_read_b64_tr_b16 v[148:149], v191 offset:24576
	ds_read_b64_tr_b16 v[150:151], v191 offset:25088
	s_waitcnt lgkmcnt(9)
	v_mfma_f32_32x32x16_f16 v[64:79], v[56:59], v[124:127], v[32:47]
	v_exp_f32_e32 v88, v88
	v_exp_f32_e32 v89, v89
	v_cvt_pk_f16_f32 v140, v96, v97
	v_cvt_pk_f16_f32 v141, v98, v99
	ds_read_b64_tr_b16 v[144:145], v191 offset:28672
	ds_read_b64_tr_b16 v[146:147], v191 offset:29184
	s_waitcnt lgkmcnt(10)
	v_mfma_f32_32x32x16_f16 v[48:63], v[176:179], v[124:127], v[32:47]
	v_exp_f32_e32 v90, v90
	v_exp_f32_e32 v91, v91
	v_pk_add_f16 v128, v140, v141
	v_cvt_pk_f16_f32 v142, v100, v101
	v_cvt_pk_f16_f32 v143, v102, v103
	ds_read_b64_tr_b16 v[96:97], v191 offset:25600
	ds_read_b64_tr_b16 v[98:99], v191 offset:26112
	s_waitcnt lgkmcnt(11)
	v_mfma_f32_32x32x16_f16 v[64:79], v[172:175], v[120:123], v[64:79]
	v_exp_f32_e32 v92, v92
	v_exp_f32_e32 v93, v93
	v_pk_add_f16 v129, v142, v143
	v_cvt_pk_f16_f32 v136, v104, v105
	v_cvt_pk_f16_f32 v137, v106, v107
	ds_read_b64_tr_b16 v[100:101], v191 offset:29696
	ds_read_b64_tr_b16 v[102:103], v191 offset:30208
	s_waitcnt lgkmcnt(12)
	v_mfma_f32_32x32x16_f16 v[48:63], v[168:171], v[120:123], v[48:63]
	v_exp_f32_e32 v94, v94
	v_exp_f32_e32 v95, v95
	v_pk_add_f16 v128, v128, v129
	v_cvt_pk_f16_f32 v138, v108, v109
	v_cvt_pk_f16_f32 v139, v110, v111
	v_pk_add_f16 v172, v136, v137
	s_add_i32 m0, s29, s24
	s_min_u32 s31, s26, 27
	s_lshl_b32 s31, s31, 13
	s_add_u32 s31, s14, s31
	s_addc_u32 s35, s15, 0
	s_add_u32 s34, s31, 0x8000
	s_addc_u32 s35, s35, 0
	global_load_lds_dwordx4 v189, s[34:35]
	ds_read_b64_tr_b16 v[104:105], v191 offset:26624
	ds_read_b64_tr_b16 v[106:107], v191 offset:27136
	s_waitcnt lgkmcnt(13)
	v_mfma_f32_32x32x16_f16 v[64:79], v[164:167], v[116:119], v[64:79]
	v_pk_add_f16 v108, v138, v139
	v_cvt_pk_f16_f32 v132, v80, v81
	v_cvt_pk_f16_f32 v133, v82, v83
	ds_read_b64_tr_b16 v[80:81], v191 offset:30720
	ds_read_b64_tr_b16 v[82:83], v191 offset:31232
	s_waitcnt lgkmcnt(14)
	v_mfma_f32_32x32x16_f16 v[48:63], v[160:163], v[116:119], v[48:63]
	v_pk_add_f16 v129, v172, v108
	v_cvt_pk_f16_f32 v134, v84, v85
	v_cvt_pk_f16_f32 v135, v86, v87
	v_pk_add_f16 v164, v132, v133
	s_add_i32 m0, s33, s25
	s_add_u32 s34, s27, 0x4000
	s_addc_u32 s35, s28, 0
	global_load_lds_dwordx4 v189, s[34:35]
	ds_read_b64_tr_b16 v[108:109], v191 offset:27648
	ds_read_b64_tr_b16 v[110:111], v191 offset:28160
	s_waitcnt lgkmcnt(14)
	v_mfma_f32_32x32x16_f16 v[64:79], v[156:159], v[112:115], v[64:79]
	v_pk_add_f16 v161, v128, v129
	v_cvt_pk_f16_f32 v128, v88, v89
	v_cvt_pk_f16_f32 v129, v90, v91
	v_pk_add_f16 v160, v134, v135
	ds_read_b64_tr_b16 v[84:85], v191 offset:31744
	ds_read_b64_tr_b16 v[86:87], v191 offset:32256
	v_mfma_f32_32x32x16_f16 v[48:63], v[152:155], v[112:115], v[48:63]
	v_pk_add_f16 v88, v128, v129
	v_pk_add_f16 v89, v164, v160
	v_cvt_pk_f16_f32 v130, v92, v93
	v_cvt_pk_f16_f32 v131, v94, v95
	s_and_b64 vcc, exec, s[16:17]
	v_pk_add_f16 v89, v161, v89
	v_pk_add_f16 v90, v130, v131
	s_cbranch_vccnz .LBB2_13
	v_pk_add_f16 v91, v88, v90
	v_max3_f32 v93, v64, v65, v48
	v_max3_f32 v94, v66, v67, v49
	s_mov_b64 s[8:9], 0
	v_pk_add_f16 v91, v89, v91
	s_nop 0
	v_cvt_f32_f16_e32 v92, v91
	v_cvt_f32_f16_sdwa v91, v91 dst_sel:DWORD dst_unused:UNUSED_PAD src0_sel:WORD_1
	v_add_f32_e32 v91, v91, v92
	v_add_f32_e32 v188, v188, v91
	v_max3_f32 v91, v93, v50, v51
	v_max3_f32 v92, v94, v70, v71
	s_nop 0
	v_max3_f32 v91, v91, v68, v69
	v_max3_f32 v92, v92, v54, v55
	s_nop 0
	v_max3_f32 v91, v91, v52, v53
	v_max3_f32 v92, v92, v74, v75
	s_nop 0
	v_max3_f32 v91, v91, v72, v73
	v_max3_f32 v92, v92, v58, v59
	s_nop 0
	v_max3_f32 v91, v91, v56, v57
	v_max3_f32 v92, v92, v78, v79
	s_nop 0
	v_max3_f32 v91, v91, v76, v77
	v_max3_f32 v92, v92, v62, v63
	s_nop 0
	v_max3_f32 v91, v91, v60, v61
	s_nop 0
	v_max_f32 v91, v91, v92
	s_nop 0
	v_mov_b32_e32 v92, v91
	s_nop 1
	v_permlane32_swap_b32_e32 v91, v92
	v_max_f32 v91, v91, v92
	s_nop 0
	v_cmp_lt_f32_e32 vcc, s30, v91
	s_cbranch_vccnz .LBB2_22
